# DSA attention unit set-up de-waterfall: selection-mask rebuild loads in two groups of four instead of eight serial round trips, bucket-id table load shares a round trip, pre-claim atomic consumed at i
# baseline (speedup 1.0000x reference)
.LBB0_1616:
	s_cmp_eq_u32 s33, 1
	s_mov_b64 s[4:5], -1
	s_cbranch_scc1 .LBB0_1705
	v_mov_b32_e32 v20, v233
	v_mov_b32_e32 v23, 0
	v_cmp_eq_u32_e32 vcc, 0, v20
	v_readfirstlane_b32 s41, v20
	s_and_b64 s[4:5], s[30:31], vcc
	s_and_saveexec_b64 s[10:11], s[4:5]
	s_cbranch_execz .LBB0_1621
	s_mov_b64 s[34:35], exec
	v_mbcnt_lo_u32_b32 v2, s34, 0
	v_mbcnt_hi_u32_b32 v2, s35, v2
	v_cmp_eq_u32_e32 vcc, 0, v2
	s_and_saveexec_b64 s[12:13], vcc
	s_cbranch_execz .LBB0_1620
	s_bcnt1_i32_b64 s7, s[34:35]
	v_mov_b32_e32 v97, s7
	global_atomic_add v97, v3, v97, s[14:15] sc0
.LBB0_1620:
	s_or_b64 exec, exec, s[12:13]
.LBB0_1621:
	s_or_b64 exec, exec, s[10:11]
	s_ashr_i32 s33, s41, 6
	s_lshl_b32 s7, s33, 5
	s_lshl_b32 s13, s82, 6
	s_and_b32 s42, s7, 32
	v_and_b32_e32 v170, 31, v20
	s_or_b32 s7, s42, s13
	s_lshl_b32 s12, s83, 11
	v_or_b32_e32 v171, s7, v170
	v_add_u32_e32 v4, s12, v171
	s_ashr_i32 s40, s41, 7
	v_ashrrev_i32_e32 v5, 31, v4
	v_lshlrev_b64 v[4:5], 9, v[4:5]
	s_lshl_b32 s10, s40, 6
	v_bfe_u32 v22, v20, 5, 1
	v_lshl_add_u64 v[4:5], s[16:17], 0, v[4:5]
	s_ashr_i32 s11, s10, 31
	v_lshl_add_u64 v[4:5], s[10:11], 1, v[4:5]
	v_lshlrev_b32_e32 v2, 4, v22
	v_add_u32_e32 v26, 0x200, v20
	v_add_u32_e32 v25, 0x400, v20
	v_lshl_add_u64 v[164:165], v[4:5], 0, v[2:3]
	v_min_i32_e32 v4, 0x83f, v26
	v_min_i32_e32 v6, 0x83f, v25
	v_ashrrev_i32_e32 v5, 31, v4
	v_ashrrev_i32_e32 v7, 31, v6
	v_lshl_add_u64 v[4:5], v[4:5], 4, s[28:29]
	v_lshl_add_u64 v[6:7], v[6:7], 4, s[28:29]
	v_add_u32_e32 v24, 0x600, v20
	v_add_u32_e32 v2, 0x800, v20
	global_load_dwordx4 v[148:151], v[164:165], off
	global_load_dwordx4 v[152:155], v[164:165], off offset:32
	global_load_dwordx4 v[156:159], v[164:165], off offset:64
	global_load_dwordx4 v[160:163], v[164:165], off offset:96
	global_load_dwordx4 v[16:19], v[4:5], off
	global_load_dwordx4 v[8:11], v[6:7], off
	v_min_i32_e32 v4, 0x83f, v24
	v_min_i32_e32 v6, 0x83f, v2
	v_ashrrev_i32_e32 v5, 31, v4
	v_ashrrev_i32_e32 v7, 31, v6
	v_lshl_add_u64 v[4:5], v[4:5], 4, s[28:29]
	v_lshl_add_u64 v[6:7], v[6:7], 4, s[28:29]
	global_load_dwordx4 v[12:15], v[4:5], off
	s_nop 0
	global_load_dwordx4 v[4:7], v[6:7], off
	s_movk_i32 s10, 0x840
	v_cmp_gt_i32_e32 vcc, s10, v20
	s_and_saveexec_b64 s[10:11], vcc
	s_cbranch_execz .LBB0_1623
	v_ashrrev_i32_e32 v21, 31, v20
	v_lshl_add_u64 v[28:29], v[20:21], 4, s[28:29]
	global_load_dwordx4 v[28:31], v[28:29], off
	v_lshl_add_u32 v21, v20, 4, s70
	s_waitcnt vmcnt(0)
	ds_write_b128 v21, v[28:31]

.LBB0_1631:
	s_or_b64 exec, exec, s[10:11]
	s_movk_i32 s10, 0x84
	v_cmp_gt_i32_e32 vcc, s10, v20
	s_and_saveexec_b64 s[10:11], vcc
	s_cbranch_execz .LBB0_1633
.LBB0_1633:
	s_or_b64 exec, exec, s[10:11]
	v_and_b32_e32 v21, 63, v20
	s_movk_i32 s10, 0x1000
	v_cmp_gt_i32_e32 vcc, s10, v20
	v_lshlrev_b32_e32 v2, 4, v21
	s_and_saveexec_b64 s[34:35], vcc
	s_cbranch_execz .LBB0_1638
	s_lshl_b32 s10, s82, 1
	s_add_i32 s36, s10, 2
	s_add_i32 s10, s12, s13
	s_ashr_i32 s10, s10, 2
	s_ashr_i32 s11, s10, 31
	s_lshl_b64 s[10:11], s[10:11], 10
	v_readlane_b32 s13, v255, 23
	s_add_u32 s10, s13, s10
	v_readlane_b32 s13, v255, 44
	s_addc_u32 s11, s13, s11
	v_cmp_gt_u32_e32 vcc, s36, v21
	s_waitcnt vmcnt(0)
	v_lshl_add_u64 v[4:5], s[10:11], 0, v[2:3]
	v_lshl_add_u32 v6, v21, 2, s81
	s_mov_b64 s[36:37], 0
	s_branch .LBB0_1636
.LBB0_1636:
	s_mov_b64 s[36:37], vcc
	s_and_saveexec_b64 s[10:11], vcc
	v_ashrrev_i32_e32 v90, 8, v20
	v_lshlrev_b32_e32 v90, 10, v90
	v_mov_b32_e32 v91, v3
	v_lshl_add_u64 v[90:91], v[4:5], 0, v[90:91]
	v_add_co_u32_e32 v98, vcc, 0x1000, v90
	v_addc_co_u32_e32 v99, vcc, 0, v91, vcc
	global_load_dwordx4 v[100:103], v[90:91], off
	global_load_dwordx4 v[104:107], v[90:91], off offset:2048
	global_load_dwordx4 v[108:111], v[98:99], off
	global_load_dwordx4 v[112:115], v[98:99], off offset:2048
	s_mov_b64 exec, s[10:11]
	v_cmp_gt_i32_e32 vcc, 0x84, v233
	s_and_saveexec_b64 s[10:11], vcc
	v_lshlrev_b32_e32 v92, 4, v233
	v_mov_b32_e32 v93, v3
	v_add_u32_e32 v96, s94, v92
	v_lshl_add_u64 v[92:93], s[26:27], 0, v[92:93]
	global_load_dwordx4 v[92:95], v[92:93], off
	s_waitcnt vmcnt(0)
	ds_write_b128 v96, v[92:95]
	s_mov_b64 exec, s[10:11]
	s_and_saveexec_b64 s[10:11], s[36:37]
	v_ashrrev_i32_e32 v7, 6, v20
	v_lshlrev_b32_e32 v12, 4, v7
	s_movk_i32 s13, 0x104
	v_mad_u32_u24 v13, v7, s13, v6
	v_add_co_u32_e32 v90, vcc, 0x2000, v90
	v_addc_co_u32_e32 v91, vcc, 0, v91, vcc
	v_add_co_u32_e32 v98, vcc, 0x2000, v98
	v_addc_co_u32_e32 v99, vcc, 0, v99, vcc
	s_waitcnt vmcnt(0)
	v_lshrrev_b64 v[8:9], v12, v[100:101]
	v_lshrrev_b64 v[10:11], v12, v[102:103]
	v_and_b32_e32 v8, 0xffff, v8
	v_lshl_or_b32 v8, v10, 16, v8
	ds_write_b32 v13, v8 offset:0
	v_lshrrev_b64 v[8:9], v12, v[104:105]
	v_lshrrev_b64 v[10:11], v12, v[106:107]
	v_and_b32_e32 v8, 0xffff, v8
	v_lshl_or_b32 v8, v10, 16, v8
	ds_write_b32 v13, v8 offset:2080
	v_lshrrev_b64 v[8:9], v12, v[108:109]
	v_lshrrev_b64 v[10:11], v12, v[110:111]
	v_and_b32_e32 v8, 0xffff, v8
	v_lshl_or_b32 v8, v10, 16, v8
	ds_write_b32 v13, v8 offset:4160
	v_lshrrev_b64 v[8:9], v12, v[112:113]
	v_lshrrev_b64 v[10:11], v12, v[114:115]
	v_and_b32_e32 v8, 0xffff, v8
	v_lshl_or_b32 v8, v10, 16, v8
	ds_write_b32 v13, v8 offset:6240
	global_load_dwordx4 v[100:103], v[90:91], off
	global_load_dwordx4 v[104:107], v[90:91], off offset:2048
	global_load_dwordx4 v[108:111], v[98:99], off
	global_load_dwordx4 v[112:115], v[98:99], off offset:2048
	s_waitcnt vmcnt(0)
	v_lshrrev_b64 v[8:9], v12, v[100:101]
	v_lshrrev_b64 v[10:11], v12, v[102:103]
	v_and_b32_e32 v8, 0xffff, v8
	v_lshl_or_b32 v8, v10, 16, v8
	ds_write_b32 v13, v8 offset:8320
	v_lshrrev_b64 v[8:9], v12, v[104:105]
	v_lshrrev_b64 v[10:11], v12, v[106:107]
	v_and_b32_e32 v8, 0xffff, v8
	v_lshl_or_b32 v8, v10, 16, v8
	ds_write_b32 v13, v8 offset:10400
	v_lshrrev_b64 v[8:9], v12, v[108:109]
	v_lshrrev_b64 v[10:11], v12, v[110:111]
	v_and_b32_e32 v8, 0xffff, v8
	v_lshl_or_b32 v8, v10, 16, v8
	ds_write_b32 v13, v8 offset:12480
	v_lshrrev_b64 v[8:9], v12, v[112:113]
	v_lshrrev_b64 v[10:11], v12, v[114:115]
	v_and_b32_e32 v8, 0xffff, v8
	v_lshl_or_b32 v8, v10, 16, v8
	ds_write_b32 v13, v8 offset:14560
	s_mov_b64 exec, s[10:11]
.LBB0_1638:
	s_or_b64 exec, exec, s[34:35]
	s_waitcnt lgkmcnt(0)
	s_barrier
	s_waitcnt vmcnt(0)
	s_waitcnt vmcnt(7)
	s_waitcnt vmcnt(6)
	s_waitcnt vmcnt(5)
	s_waitcnt vmcnt(4)
	s_and_saveexec_b64 s[10:11], s[4:5]
	s_cbranch_execz .LBB0_1640
	s_waitcnt vmcnt(0)
	v_mov_b32_e32 v4, s69
	ds_write_b32 v4, v97
